# gather: one static priority raise (s_setprio 1) for waves 4-7 of each block for the whole expert-gather phase, reset after
# speedup vs baseline: 1.0038x; 1.0027x over previous
.LBB0_759:
	s_or_b64 exec, exec, s[6:7]
	v_readlane_b32 s8, v255, 42
	v_readlane_b32 s9, v255, 43
	s_mov_b64 s[6:7], -1
	s_and_b64 vcc, exec, s[8:9]
	s_waitcnt lgkmcnt(0)
	s_barrier
	s_cbranch_vccz .LBB0_766
	v_readlane_b32 s10, v253, 0
	v_readlane_b32 s11, v253, 1
	v_mov_b32_e32 v3, v175
	v_readlane_b32 s6, v253, 8
	v_ashrrev_i32_e32 v0, 6, v3
	s_nop 0
	v_readfirstlane_b32 s32, v0
	s_cmp_lt_u32 s32, 4
	s_cbranch_scc1 .Lgprio_f
	s_setprio 1
.Lgprio_f:
	v_add_u32_e32 v0, s6, v0
	v_cmp_gt_i32_e32 vcc, s87, v0
	s_and_saveexec_b64 s[6:7], vcc
	s_mov_b32 s18, 0x800000
	s_cbranch_execz .LBB0_765
	v_ashrrev_i32_e32 v1, 31, v0
	v_and_b32_e32 v2, 15, v3
	v_lshlrev_b64 v[34:35], 9, v[0:1]
	v_lshl_add_u64 v[4:5], s[94:95], 0, v[34:35]
	v_lshlrev_b32_e32 v144, 2, v2
	v_lshl_add_u64 v[4:5], v[4:5], 0, v[144:145]
	global_load_dword v92, v[4:5], off
	v_readlane_b32 s12, v255, 7
	v_readlane_b32 s13, v255, 8
	s_lshl_b64 s[8:9], s[12:13], 17
	s_add_u32 s8, s88, s8
	s_addc_u32 s9, s89, s9
	s_lshl_b64 s[14:15], s[12:13], 23
	v_readlane_b32 s12, v253, 29
	v_readlane_b32 s13, v253, 30
	s_add_u32 s12, s12, s14
	v_and_b32_e32 v28, 63, v3
	s_addc_u32 s13, s13, s15
	v_readlane_b32 s16, v253, 27
	v_lshlrev_b32_e32 v144, 3, v28
	v_readlane_b32 s17, v253, 28
	s_add_u32 s14, s16, s14
	v_lshl_add_u64 v[6:7], s[12:13], 0, v[144:145]
	s_addc_u32 s15, s17, s15
	v_lshl_add_u64 v[4:5], s[14:15], 0, v[144:145]
	s_load_dwordx2 s[10:11], s[10:11], 0xf0
	v_lshlrev_b32_e32 v144, 5, v28
	v_and_b32_e32 v1, 32, v3
	v_cmp_eq_u32_e64 s[40:41], 0, v1
	v_and_b32_e32 v1, 16, v3
	v_and_b32_e32 v93, 60, v3
	v_cmp_eq_u32_e64 s[42:43], 0, v1
	v_and_b32_e32 v1, 8, v3
	v_cmp_eq_u32_e64 s[44:45], 0, v1
	v_and_b32_e32 v1, 4, v3
	v_or_b32_e32 v34, v34, v93
	v_cmp_eq_u32_e64 s[46:47], 0, v1
	s_waitcnt vmcnt(0)
	v_readlane_b32 s12, v92, 0
	s_ashr_i32 s13, s12, 31
	s_lshl_b64 s[12:13], s[12:13], 9
	v_lshl_add_u64 v[8:9], v[4:5], 0, s[12:13]
	v_lshl_add_u64 v[10:11], v[6:7], 0, s[12:13]
	v_readlane_b32 s12, v92, 1
	s_ashr_i32 s13, s12, 31
	s_lshl_b64 s[12:13], s[12:13], 9
	v_lshl_add_u64 v[12:13], v[6:7], 0, s[12:13]
	global_load_dwordx2 v[8:9], v[8:9], off
	s_nop 0
	global_load_dwordx2 v[82:83], v[10:11], off
	global_load_dwordx2 v[80:81], v[12:13], off
	v_lshl_add_u64 v[10:11], v[4:5], 0, s[12:13]
	v_readlane_b32 s12, v92, 2
	s_ashr_i32 s13, s12, 31
	s_lshl_b64 s[12:13], s[12:13], 9
	v_lshl_add_u64 v[12:13], v[4:5], 0, s[12:13]
	v_lshl_add_u64 v[14:15], v[6:7], 0, s[12:13]
	v_readlane_b32 s12, v92, 3
	s_ashr_i32 s13, s12, 31
	s_lshl_b64 s[12:13], s[12:13], 9
	v_lshl_add_u64 v[16:17], v[6:7], 0, s[12:13]
	global_load_dwordx2 v[10:11], v[10:11], off
	s_nop 0
	global_load_dwordx2 v[12:13], v[12:13], off
	s_nop 0
	global_load_dwordx2 v[78:79], v[14:15], off
	global_load_dwordx2 v[76:77], v[16:17], off
	v_lshl_add_u64 v[14:15], v[4:5], 0, s[12:13]
	v_readlane_b32 s12, v92, 4
	s_ashr_i32 s13, s12, 31
	s_lshl_b64 s[12:13], s[12:13], 9
	v_lshl_add_u64 v[16:17], v[4:5], 0, s[12:13]
	v_lshl_add_u64 v[18:19], v[6:7], 0, s[12:13]
	v_readlane_b32 s12, v92, 5
	s_ashr_i32 s13, s12, 31
	s_lshl_b64 s[12:13], s[12:13], 9
	v_lshl_add_u64 v[20:21], v[6:7], 0, s[12:13]
	global_load_dwordx2 v[14:15], v[14:15], off
	s_nop 0
	global_load_dwordx2 v[16:17], v[16:17], off
	s_nop 0
	global_load_dwordx2 v[74:75], v[18:19], off
	global_load_dwordx2 v[70:71], v[20:21], off
	v_lshl_add_u64 v[18:19], v[4:5], 0, s[12:13]
	v_readlane_b32 s12, v92, 6
	s_ashr_i32 s13, s12, 31
	s_lshl_b64 s[12:13], s[12:13], 9
	v_lshl_add_u64 v[20:21], v[4:5], 0, s[12:13]
	v_lshl_add_u64 v[22:23], v[6:7], 0, s[12:13]
	v_readlane_b32 s12, v92, 7
	s_ashr_i32 s13, s12, 31
	s_lshl_b64 s[12:13], s[12:13], 9
	v_lshl_add_u64 v[24:25], v[6:7], 0, s[12:13]
	global_load_dwordx2 v[18:19], v[18:19], off
	s_nop 0
	global_load_dwordx2 v[20:21], v[20:21], off
	s_nop 0
	global_load_dwordx2 v[68:69], v[22:23], off
	global_load_dwordx2 v[64:65], v[24:25], off
	v_lshl_add_u64 v[22:23], v[4:5], 0, s[12:13]
	v_readlane_b32 s12, v92, 8
	s_ashr_i32 s13, s12, 31
	s_lshl_b64 s[12:13], s[12:13], 9
	v_lshl_add_u64 v[24:25], v[4:5], 0, s[12:13]
	v_lshl_add_u64 v[26:27], v[6:7], 0, s[12:13]
	v_readlane_b32 s12, v92, 9
	s_ashr_i32 s13, s12, 31
	s_lshl_b64 s[12:13], s[12:13], 9
	global_load_dwordx2 v[22:23], v[22:23], off
	s_nop 0
	global_load_dwordx2 v[24:25], v[24:25], off
	s_nop 0
	global_load_dwordx2 v[62:63], v[26:27], off
	v_lshl_add_u64 v[26:27], v[4:5], 0, s[12:13]
	global_load_dwordx2 v[38:39], v[26:27], off
	v_lshl_add_u64 v[26:27], v[6:7], 0, s[12:13]
	v_readlane_b32 s12, v92, 10
	s_ashr_i32 s13, s12, 31
	s_lshl_b64 s[12:13], s[12:13], 9
	global_load_dwordx2 v[66:67], v[26:27], off
	v_lshl_add_u64 v[26:27], v[4:5], 0, s[12:13]
	global_load_dwordx2 v[50:51], v[26:27], off
	v_lshl_add_u64 v[26:27], v[6:7], 0, s[12:13]
	v_readlane_b32 s12, v92, 11
	s_ashr_i32 s13, s12, 31
	s_lshl_b64 s[12:13], s[12:13], 9
	global_load_dwordx2 v[60:61], v[26:27], off
	v_lshl_add_u64 v[26:27], v[4:5], 0, s[12:13]
	global_load_dwordx2 v[48:49], v[26:27], off
	v_lshl_add_u64 v[26:27], v[6:7], 0, s[12:13]
	v_readlane_b32 s12, v92, 12
	s_ashr_i32 s13, s12, 31
	s_lshl_b64 s[12:13], s[12:13], 9
	global_load_dwordx2 v[58:59], v[26:27], off
	v_lshl_add_u64 v[26:27], v[4:5], 0, s[12:13]
	global_load_dwordx2 v[46:47], v[26:27], off
	v_lshl_add_u64 v[26:27], v[6:7], 0, s[12:13]
	v_readlane_b32 s12, v92, 13
	s_ashr_i32 s13, s12, 31
	s_lshl_b64 s[12:13], s[12:13], 9
	global_load_dwordx2 v[56:57], v[26:27], off
	v_lshl_add_u64 v[26:27], v[4:5], 0, s[12:13]
	global_load_dwordx2 v[44:45], v[26:27], off
	v_lshl_add_u64 v[26:27], v[6:7], 0, s[12:13]
	v_readlane_b32 s12, v92, 14
	s_ashr_i32 s13, s12, 31
	s_lshl_b64 s[12:13], s[12:13], 9
	global_load_dwordx2 v[54:55], v[26:27], off
	v_lshl_add_u64 v[26:27], v[4:5], 0, s[12:13]
	global_load_dwordx2 v[42:43], v[26:27], off
	v_lshl_add_u64 v[26:27], v[6:7], 0, s[12:13]
	v_readlane_b32 s12, v92, 15
	s_ashr_i32 s13, s12, 31
	s_lshl_b64 s[12:13], s[12:13], 9
	global_load_dwordx2 v[52:53], v[26:27], off
	v_lshl_add_u64 v[26:27], v[4:5], 0, s[12:13]
	global_load_dwordx2 v[40:41], v[26:27], off
	v_lshl_add_u64 v[26:27], v[6:7], 0, s[12:13]
	global_load_dwordx2 v[36:37], v[26:27], off
	v_readlane_b32 s12, v253, 15
	v_readlane_b32 s13, v253, 16
	s_nop 1
	v_lshl_add_u64 v[26:27], s[12:13], 0, v[144:145]
	v_readlane_b32 s12, v253, 13
	v_lshlrev_b32_e32 v144, 6, v28
	v_readlane_b32 s13, v253, 14
	s_waitcnt lgkmcnt(0)
	v_lshl_add_u64 v[30:31], s[10:11], 0, v[144:145]
	v_readlane_b32 s10, v253, 23
	v_lshl_add_u64 v[28:29], s[12:13], 0, v[144:145]
	v_readlane_b32 s12, v253, 2
	v_readlane_b32 s13, v253, 3
	v_readlane_b32 s11, v253, 24
	v_readlane_b32 s14, v253, 4
	v_lshl_add_u64 v[32:33], s[12:13], 0, v[144:145]
	v_lshl_add_u64 v[34:35], s[10:11], 0, v[34:35]
	s_mov_b64 s[10:11], 0
	v_lshlrev_b32_e32 v144, 2, v2
	v_readlane_b32 s15, v253, 5
	global_load_dwordx4 v[124:127], v[30:31], off
	global_load_dwordx4 v[128:131], v[30:31], off offset:16
	global_load_dwordx4 v[132:135], v[30:31], off offset:32
	global_load_dwordx4 v[136:139], v[30:31], off offset:48
	v_readfirstlane_b32 s62, v4
	v_readfirstlane_b32 s63, v5
	v_readfirstlane_b32 s64, v6
	v_readfirstlane_b32 s65, v7
	v_and_b32_e32 v121, 63, v175
	v_lshlrev_b32_e32 v121, 3, v121

.LBB0_765:
	s_setprio 0
	s_or_b64 exec, exec, s[6:7]
	v_readlane_b32 s30, v255, 15
	v_readlane_b32 s34, v255, 17
	v_readlane_b32 s44, v255, 19
	v_readlane_b32 s46, v255, 21
	v_readlane_b32 s22, v255, 23
	s_mov_b64 s[6:7], 0
	v_readlane_b32 s31, v255, 16
	v_readlane_b32 s35, v255, 18
	v_readlane_b32 s45, v255, 20
	v_readlane_b32 s47, v255, 22
	v_readlane_b32 s23, v255, 24
	s_movk_i32 s27, 0x1200

.LBB0_767:
	v_readlane_b32 s8, v253, 0
	v_readlane_b32 s9, v253, 1
	v_mov_b32_e32 v3, v175
	v_readlane_b32 s6, v253, 8
	v_ashrrev_i32_e32 v0, 6, v3
	s_nop 0
	v_readfirstlane_b32 s32, v0
	s_cmp_lt_u32 s32, 4
	s_cbranch_scc1 .Lgprio_l
	s_setprio 1
.Lgprio_l:
	v_add_u32_e32 v0, s6, v0
	v_cmp_gt_i32_e32 vcc, s87, v0
	s_and_saveexec_b64 s[6:7], vcc
	s_mov_b32 s12, 0x800000
	s_cbranch_execz .LBB0_772
	v_ashrrev_i32_e32 v1, 31, v0
	v_and_b32_e32 v2, 15, v3
	v_lshlrev_b64 v[4:5], 9, v[0:1]
	v_lshl_add_u64 v[8:9], s[94:95], 0, v[4:5]
	v_lshlrev_b32_e32 v144, 2, v2
	v_lshl_add_u64 v[8:9], v[8:9], 0, v[144:145]
	global_load_dword v96, v[8:9], off
	v_and_b32_e32 v6, 63, v3
	v_readlane_b32 s10, v253, 27
	v_lshlrev_b32_e32 v144, 3, v6
	v_readlane_b32 s11, v253, 28
	s_load_dwordx2 s[8:9], s[8:9], 0x10
	v_and_b32_e32 v1, 32, v3
	v_lshl_add_u64 v[16:17], s[10:11], 0, v[144:145]
	v_readlane_b32 s10, v253, 29
	v_readlane_b32 s11, v253, 30
	v_cmp_eq_u32_e64 s[40:41], 0, v1
	v_and_b32_e32 v1, 16, v3
	v_lshl_add_u64 v[18:19], s[10:11], 0, v[144:145]
	v_lshlrev_b32_e32 v144, 5, v6
	v_and_b32_e32 v97, 60, v3
	v_cmp_eq_u32_e64 s[42:43], 0, v1
	v_and_b32_e32 v1, 8, v3
	v_cmp_eq_u32_e64 s[44:45], 0, v1
	v_and_b32_e32 v1, 4, v3
	v_or_b32_e32 v4, v4, v97
	v_cmp_eq_u32_e64 s[46:47], 0, v1
	s_waitcnt vmcnt(0)
	v_readlane_b32 s10, v96, 0
	s_ashr_i32 s11, s10, 31
	s_lshl_b64 s[10:11], s[10:11], 9
	v_lshl_add_u64 v[8:9], v[16:17], 0, s[10:11]
	global_load_dwordx2 v[20:21], v[8:9], off
	v_lshl_add_u64 v[8:9], v[18:19], 0, s[10:11]
	v_readlane_b32 s10, v96, 1
	s_ashr_i32 s11, s10, 31
	s_lshl_b64 s[10:11], s[10:11], 9
	global_load_dwordx2 v[92:93], v[8:9], off
	v_lshl_add_u64 v[8:9], v[16:17], 0, s[10:11]
	global_load_dwordx2 v[22:23], v[8:9], off
	v_lshl_add_u64 v[8:9], v[18:19], 0, s[10:11]
	v_readlane_b32 s10, v96, 2
	s_ashr_i32 s11, s10, 31
	s_lshl_b64 s[10:11], s[10:11], 9
	global_load_dwordx2 v[90:91], v[8:9], off
	v_lshl_add_u64 v[8:9], v[16:17], 0, s[10:11]
	global_load_dwordx2 v[24:25], v[8:9], off
	v_lshl_add_u64 v[8:9], v[18:19], 0, s[10:11]
	v_readlane_b32 s10, v96, 3
	s_ashr_i32 s11, s10, 31
	s_lshl_b64 s[10:11], s[10:11], 9
	global_load_dwordx2 v[88:89], v[8:9], off
	v_lshl_add_u64 v[8:9], v[16:17], 0, s[10:11]
	global_load_dwordx2 v[26:27], v[8:9], off
	v_lshl_add_u64 v[8:9], v[18:19], 0, s[10:11]
	v_readlane_b32 s10, v96, 4
	s_ashr_i32 s11, s10, 31
	s_lshl_b64 s[10:11], s[10:11], 9
	global_load_dwordx2 v[86:87], v[8:9], off
	v_lshl_add_u64 v[8:9], v[16:17], 0, s[10:11]
	global_load_dwordx2 v[28:29], v[8:9], off
	v_lshl_add_u64 v[8:9], v[18:19], 0, s[10:11]
	v_readlane_b32 s10, v96, 5
	s_ashr_i32 s11, s10, 31
	s_lshl_b64 s[10:11], s[10:11], 9
	global_load_dwordx2 v[84:85], v[8:9], off
	v_lshl_add_u64 v[8:9], v[16:17], 0, s[10:11]
	global_load_dwordx2 v[30:31], v[8:9], off
	v_lshl_add_u64 v[8:9], v[18:19], 0, s[10:11]
	v_readlane_b32 s10, v96, 6
	s_ashr_i32 s11, s10, 31
	s_lshl_b64 s[10:11], s[10:11], 9
	global_load_dwordx2 v[82:83], v[8:9], off
	v_lshl_add_u64 v[8:9], v[16:17], 0, s[10:11]
	global_load_dwordx2 v[32:33], v[8:9], off
	v_lshl_add_u64 v[8:9], v[18:19], 0, s[10:11]
	v_readlane_b32 s10, v96, 7
	s_ashr_i32 s11, s10, 31
	s_lshl_b64 s[10:11], s[10:11], 9
	global_load_dwordx2 v[80:81], v[8:9], off
	v_lshl_add_u64 v[8:9], v[16:17], 0, s[10:11]
	global_load_dwordx2 v[34:35], v[8:9], off
	v_lshl_add_u64 v[8:9], v[18:19], 0, s[10:11]
	v_readlane_b32 s10, v96, 8
	s_ashr_i32 s11, s10, 31
	s_lshl_b64 s[10:11], s[10:11], 9
	global_load_dwordx2 v[78:79], v[8:9], off
	v_lshl_add_u64 v[8:9], v[16:17], 0, s[10:11]
	global_load_dwordx2 v[36:37], v[8:9], off
	v_lshl_add_u64 v[8:9], v[18:19], 0, s[10:11]
	v_readlane_b32 s10, v96, 9
	s_ashr_i32 s11, s10, 31
	s_lshl_b64 s[10:11], s[10:11], 9
	global_load_dwordx2 v[76:77], v[8:9], off
	v_lshl_add_u64 v[8:9], v[16:17], 0, s[10:11]
	global_load_dwordx2 v[38:39], v[8:9], off
	v_lshl_add_u64 v[8:9], v[18:19], 0, s[10:11]
	v_readlane_b32 s10, v96, 10
	s_ashr_i32 s11, s10, 31
	s_lshl_b64 s[10:11], s[10:11], 9
	global_load_dwordx2 v[70:71], v[8:9], off
	v_lshl_add_u64 v[8:9], v[16:17], 0, s[10:11]
	global_load_dwordx2 v[40:41], v[8:9], off
	v_lshl_add_u64 v[8:9], v[18:19], 0, s[10:11]
	v_readlane_b32 s10, v96, 11
	s_ashr_i32 s11, s10, 31
	s_lshl_b64 s[10:11], s[10:11], 9
	global_load_dwordx2 v[66:67], v[8:9], off
	v_lshl_add_u64 v[8:9], v[16:17], 0, s[10:11]
	global_load_dwordx2 v[60:61], v[8:9], off
	v_lshl_add_u64 v[8:9], v[18:19], 0, s[10:11]
	v_readlane_b32 s10, v96, 12
	s_ashr_i32 s11, s10, 31
	s_lshl_b64 s[10:11], s[10:11], 9
	global_load_dwordx2 v[72:73], v[8:9], off
	v_lshl_add_u64 v[8:9], v[16:17], 0, s[10:11]
	global_load_dwordx2 v[58:59], v[8:9], off
	v_lshl_add_u64 v[8:9], v[18:19], 0, s[10:11]
	v_readlane_b32 s10, v96, 13
	s_ashr_i32 s11, s10, 31
	s_lshl_b64 s[10:11], s[10:11], 9
	global_load_dwordx2 v[68:69], v[8:9], off
	v_lshl_add_u64 v[8:9], v[16:17], 0, s[10:11]
	global_load_dwordx2 v[56:57], v[8:9], off
	v_lshl_add_u64 v[8:9], v[18:19], 0, s[10:11]
	v_readlane_b32 s10, v96, 14
	s_ashr_i32 s11, s10, 31
	s_lshl_b64 s[10:11], s[10:11], 9
	global_load_dwordx2 v[64:65], v[8:9], off
	v_lshl_add_u64 v[8:9], v[16:17], 0, s[10:11]
	global_load_dwordx2 v[54:55], v[8:9], off
	v_lshl_add_u64 v[8:9], v[18:19], 0, s[10:11]
	v_readlane_b32 s10, v96, 15
	s_ashr_i32 s11, s10, 31
	s_lshl_b64 s[10:11], s[10:11], 9
	global_load_dwordx2 v[62:63], v[8:9], off
	v_lshl_add_u64 v[8:9], v[16:17], 0, s[10:11]
	global_load_dwordx2 v[52:53], v[8:9], off
	v_lshl_add_u64 v[8:9], v[18:19], 0, s[10:11]
	global_load_dwordx2 v[50:51], v[8:9], off
	v_readlane_b32 s10, v253, 15
	v_readlane_b32 s11, v253, 16
	s_nop 1
	v_lshl_add_u64 v[42:43], s[10:11], 0, v[144:145]
	v_lshlrev_b32_e32 v144, 6, v6
	s_waitcnt lgkmcnt(0)
	v_lshl_add_u64 v[6:7], s[8:9], 0, v[144:145]
	s_mov_b64 s[8:9], 0x1000
	v_readlane_b32 s10, v253, 13
	v_lshl_add_u64 v[46:47], v[6:7], 0, s[8:9]
	v_readlane_b32 s8, v253, 23
	v_readlane_b32 s11, v253, 14
	v_readlane_b32 s9, v253, 24
	s_nop 0
	v_lshl_add_u64 v[44:45], s[10:11], 0, v[144:145]
	v_lshl_add_u64 v[48:49], s[8:9], 0, v[4:5]
	s_mov_b64 s[8:9], 0
	v_lshlrev_b32_e32 v144, 2, v2
	v_readfirstlane_b32 s62, v16
	v_readfirstlane_b32 s63, v17
	v_readfirstlane_b32 s64, v18
	v_readfirstlane_b32 s65, v19
	v_and_b32_e32 v121, 63, v175
	v_lshlrev_b32_e32 v121, 3, v121

.LBB0_772:
	s_setprio 0
	s_or_b64 exec, exec, s[6:7]
	s_waitcnt vmcnt(0)
	s_barrier
	s_mov_b64 s[6:7], exec
	v_readlane_b32 s8, v253, 6
	v_readlane_b32 s9, v253, 7
	v_readlane_b32 s30, v255, 15
	v_readlane_b32 s34, v255, 17
	v_readlane_b32 s44, v255, 19
	v_readlane_b32 s46, v255, 21
	v_readlane_b32 s22, v255, 23
	s_and_b64 s[8:9], s[6:7], s[8:9]
	v_readlane_b32 s31, v255, 16
	v_readlane_b32 s35, v255, 18
	v_readlane_b32 s45, v255, 20
	v_readlane_b32 s47, v255, 22
	v_readlane_b32 s23, v255, 24
	s_movk_i32 s27, 0x1200
	s_mov_b64 exec, s[8:9]
	s_cbranch_execnz .LBB0_773
	s_getpc_b64 s[98:99]
